# back-edge rotation of the two MoE main K-loops (counter updates + next tile's first-fragment addresses computed before the end-of-tile barrier); on top of the silu staging rewrite and nt loads
# speedup vs baseline: 1.0163x; 1.0034x over previous
.Lrot_m1:
	ds_read_b64_tr_b16 v[222:223], v246
	ds_read_b64_tr_b16 v[224:225], v246 offset:2048
	ds_read_b64_tr_b16 v[226:227], v250
	ds_read_b64_tr_b16 v[228:229], v250 offset:2048
	ds_read_b128 v[162:165], v247
	ds_read_b128 v[166:169], v247 offset:2048
	ds_read_b64_tr_b16 v[230:231], v252
	ds_read_b64_tr_b16 v[232:233], v252 offset:2048
	ds_read_b64_tr_b16 v[234:235], v254
	ds_read_b64_tr_b16 v[236:237], v254 offset:2048
	s_waitcnt lgkmcnt(5)
	v_mfma_f32_16x16x32_bf16 v[62:65], v[222:225], v[162:165], v[62:65]
	ds_read_b128 v[238:241], v247 offset:4096
	s_and_b32 s88, s39, 0x8000
	s_add_i32 s89, s38, s85
	v_mfma_f32_16x16x32_bf16 v[58:61], v[226:229], v[162:165], v[58:61]
	s_mov_b32 s90, m0
	s_mov_b32 m0, s89
	s_nop 0
	global_load_lds_dwordx4 v221, s[18:19]
	s_mov_b32 m0, s90
	s_waitcnt lgkmcnt(3)
	v_mfma_f32_16x16x32_bf16 v[54:57], v[230:233], v[162:165], v[54:57]
	s_waitcnt lgkmcnt(1)
	v_mfma_f32_16x16x32_bf16 v[42:45], v[234:237], v[162:165], v[42:45]
	v_mfma_f32_16x16x32_bf16 v[50:53], v[222:225], v[166:169], v[50:53]
	ds_read_b128 v[162:165], v247 offset:6144
	s_add_i32 s90, s89, 0x2000
	s_mov_b32 s91, m0
	s_mov_b32 m0, s90
	s_nop 0
	global_load_lds_dwordx4 v220, s[18:19]
	s_mov_b32 m0, s91
	v_mfma_f32_16x16x32_bf16 v[46:49], v[226:229], v[166:169], v[46:49]
	v_mfma_f32_16x16x32_bf16 v[38:41], v[230:233], v[166:169], v[38:41]
	v_mfma_f32_16x16x32_bf16 v[34:37], v[234:237], v[166:169], v[34:37]
	s_waitcnt lgkmcnt(1)
	v_mfma_f32_16x16x32_bf16 v[66:69], v[222:225], v[238:241], v[66:69]
	ds_read_b128 v[166:169], v247 offset:8192
	s_add_i32 s90, s89, 0x4000
	s_mov_b32 s91, m0
	s_mov_b32 m0, s90
	s_nop 0
	global_load_lds_dwordx4 v219, s[18:19]
	s_mov_b32 m0, s91
	v_mfma_f32_16x16x32_bf16 v[70:73], v[226:229], v[238:241], v[70:73]
	v_mfma_f32_16x16x32_bf16 v[74:77], v[230:233], v[238:241], v[74:77]
	v_mfma_f32_16x16x32_bf16 v[78:81], v[234:237], v[238:241], v[78:81]
	s_waitcnt lgkmcnt(1)
	v_mfma_f32_16x16x32_bf16 v[82:85], v[222:225], v[162:165], v[82:85]
	ds_read_b128 v[238:241], v247 offset:10240
	s_addk_i32 s89, 0x6000
	s_mov_b32 s90, m0
	s_mov_b32 m0, s89
	s_nop 0
	global_load_lds_dwordx4 v218, s[18:19]
	s_mov_b32 m0, s90
	v_mfma_f32_16x16x32_bf16 v[86:89], v[226:229], v[162:165], v[86:89]
	v_mfma_f32_16x16x32_bf16 v[90:93], v[230:233], v[162:165], v[90:93]
	v_mfma_f32_16x16x32_bf16 v[94:97], v[234:237], v[162:165], v[94:97]
	ds_read_b128 v[242:245], v247 offset:12288
	ds_read_b64_tr_b16 v[162:163], v246 offset:16384
	ds_read_b64_tr_b16 v[164:165], v246 offset:18432
	s_waitcnt lgkmcnt(4)
	v_mfma_f32_16x16x32_bf16 v[98:101], v[222:225], v[166:169], v[98:101]
	v_mfma_f32_16x16x32_bf16 v[102:105], v[226:229], v[166:169], v[102:105]
	v_mfma_f32_16x16x32_bf16 v[106:109], v[230:233], v[166:169], v[106:109]
	v_mfma_f32_16x16x32_bf16 v[110:113], v[234:237], v[166:169], v[110:113]
	ds_read_b128 v[246:249], v247 offset:14336
	ds_read_b64_tr_b16 v[166:167], v250 offset:16384
	ds_read_b64_tr_b16 v[168:169], v250 offset:18432
	s_waitcnt lgkmcnt(6)
	v_mfma_f32_16x16x32_bf16 v[114:117], v[222:225], v[238:241], v[114:117]
	v_mfma_f32_16x16x32_bf16 v[118:121], v[226:229], v[238:241], v[118:121]
	v_mfma_f32_16x16x32_bf16 v[122:125], v[230:233], v[238:241], v[122:125]
	v_mfma_f32_16x16x32_bf16 v[126:129], v[234:237], v[238:241], v[126:129]
	v_add_u32_e32 v200, s87, v216
	ds_read_b128 v[238:241], v200
	ds_read_b64_tr_b16 v[250:251], v252 offset:16384
	ds_read_b64_tr_b16 v[252:253], v252 offset:18432
	s_waitcnt lgkmcnt(8)
	v_mfma_f32_16x16x32_bf16 v[130:133], v[222:225], v[242:245], v[130:133]
	v_mfma_f32_16x16x32_bf16 v[134:137], v[226:229], v[242:245], v[134:137]
	v_mfma_f32_16x16x32_bf16 v[138:141], v[230:233], v[242:245], v[138:141]
	v_mfma_f32_16x16x32_bf16 v[142:145], v[234:237], v[242:245], v[142:145]
	s_waitcnt lgkmcnt(5)
	v_mfma_f32_16x16x32_bf16 v[146:149], v[222:225], v[246:249], v[146:149]
	v_mfma_f32_16x16x32_bf16 v[150:153], v[226:229], v[246:249], v[150:153]
	ds_read_b128 v[222:225], v200 offset:2048
	ds_read_b64_tr_b16 v[226:227], v254 offset:16384
	ds_read_b64_tr_b16 v[228:229], v254 offset:18432
	v_mfma_f32_16x16x32_bf16 v[154:157], v[230:233], v[246:249], v[154:157]
	v_mfma_f32_16x16x32_bf16 v[158:161], v[234:237], v[246:249], v[158:161]
	ds_read_b128 v[230:233], v200 offset:4096
	s_waitcnt lgkmcnt(6)
	v_mfma_f32_16x16x32_bf16 v[62:65], v[162:165], v[238:241], v[62:65]
	s_add_u32 s87, s83, s2
	s_waitcnt vmcnt(11)
	s_addc_u32 s90, s84, s3
	v_mfma_f32_16x16x32_bf16 v[58:61], v[166:169], v[238:241], v[58:61]
	v_cvt_pk_bf16_f32 v30, v30, v31
	v_cvt_pk_bf16_f32 v31, v32, v33
	v_add_u32_e32 v242, s88, v217
	s_waitcnt lgkmcnt(4)
	v_mfma_f32_16x16x32_bf16 v[54:57], v[250:253], v[238:241], v[54:57]
	s_add_u32 s88, s87, 0x160000
	ds_write_b64 v242, v[30:31]
	s_addc_u32 s89, s90, 0
	s_waitcnt lgkmcnt(2)
	v_mfma_f32_16x16x32_bf16 v[42:45], v[226:229], v[238:241], v[42:45]
	global_load_dwordx4 v[30:33], v199, s[88:89] nt
	v_mfma_f32_16x16x32_bf16 v[50:53], v[162:165], v[222:225], v[50:53]
	ds_read_b128 v[234:237], v200 offset:6144
	s_waitcnt vmcnt(11)
	s_add_u32 s88, s87, 0x18c000
	v_mfma_f32_16x16x32_bf16 v[46:49], v[166:169], v[222:225], v[46:49]
	v_cvt_pk_bf16_f32 v26, v26, v27
	v_cvt_pk_bf16_f32 v27, v28, v29
	ds_write_b64 v242, v[26:27] offset:8192
	v_mfma_f32_16x16x32_bf16 v[38:41], v[250:253], v[222:225], v[38:41]
	s_addc_u32 s89, s90, 0
	global_load_dwordx4 v[26:29], v199, s[88:89] nt
	v_mfma_f32_16x16x32_bf16 v[34:37], v[226:229], v[222:225], v[34:37]
	s_waitcnt lgkmcnt(3)
	v_mfma_f32_16x16x32_bf16 v[66:69], v[162:165], v[230:233], v[66:69]
	ds_read_b128 v[222:225], v200 offset:8192
	s_waitcnt vmcnt(11)
	s_add_u32 s88, s87, 0x1b8000
	v_mfma_f32_16x16x32_bf16 v[70:73], v[166:169], v[230:233], v[70:73]
	v_cvt_pk_bf16_f32 v22, v22, v23
	v_cvt_pk_bf16_f32 v23, v24, v25
	ds_write_b64 v242, v[22:23] offset:16384
	v_mfma_f32_16x16x32_bf16 v[74:77], v[250:253], v[230:233], v[74:77]
	s_addc_u32 s89, s90, 0
	global_load_dwordx4 v[22:25], v199, s[88:89] nt
	v_mfma_f32_16x16x32_bf16 v[78:81], v[226:229], v[230:233], v[78:81]
	s_waitcnt lgkmcnt(3)
	v_mfma_f32_16x16x32_bf16 v[82:85], v[162:165], v[234:237], v[82:85]
	ds_read_b128 v[230:233], v200 offset:10240
	s_waitcnt vmcnt(11)
	s_add_u32 s88, s87, 0x1e4000
	v_mfma_f32_16x16x32_bf16 v[86:89], v[166:169], v[234:237], v[86:89]
	v_cvt_pk_bf16_f32 v18, v18, v19
	v_cvt_pk_bf16_f32 v19, v20, v21
	ds_write_b64 v242, v[18:19] offset:24576
	v_mfma_f32_16x16x32_bf16 v[90:93], v[250:253], v[234:237], v[90:93]
	s_addc_u32 s89, s90, 0
	global_load_dwordx4 v[18:21], v199, s[88:89] nt
	v_mfma_f32_16x16x32_bf16 v[94:97], v[226:229], v[234:237], v[94:97]
	ds_read_b128 v[234:237], v200 offset:12288
	s_waitcnt lgkmcnt(4)
	v_mfma_f32_16x16x32_bf16 v[98:101], v[162:165], v[222:225], v[98:101]
	s_add_u32 s87, s40, s2
	s_waitcnt vmcnt(11)
	s_addc_u32 s90, s41, s3
	v_mfma_f32_16x16x32_bf16 v[102:105], v[166:169], v[222:225], v[102:105]
	v_cvt_pk_bf16_f32 v14, v14, v15
	v_cvt_pk_bf16_f32 v15, v16, v17
	s_add_u32 s88, s87, 0x160000
	v_mfma_f32_16x16x32_bf16 v[106:109], v[250:253], v[222:225], v[106:109]
	ds_write_b64 v242, v[14:15] offset:256
	s_addc_u32 s89, s90, 0
	global_load_dwordx4 v[14:17], v199, s[88:89] nt
	v_mfma_f32_16x16x32_bf16 v[110:113], v[226:229], v[222:225], v[110:113]
	s_waitcnt lgkmcnt(3)
	v_mfma_f32_16x16x32_bf16 v[114:117], v[162:165], v[230:233], v[114:117]
	ds_read_b128 v[222:225], v200 offset:14336
	s_waitcnt vmcnt(11)
	s_add_u32 s88, s87, 0x18c000
	v_mfma_f32_16x16x32_bf16 v[118:121], v[166:169], v[230:233], v[118:121]
	v_cvt_pk_bf16_f32 v10, v10, v11
	v_cvt_pk_bf16_f32 v11, v12, v13
	ds_write_b64 v242, v[10:11] offset:8448
	v_mfma_f32_16x16x32_bf16 v[122:125], v[250:253], v[230:233], v[122:125]
	s_addc_u32 s89, s90, 0
	global_load_dwordx4 v[10:13], v199, s[88:89] nt
	v_mfma_f32_16x16x32_bf16 v[126:129], v[226:229], v[230:233], v[126:129]
	s_waitcnt lgkmcnt(3)
	v_mfma_f32_16x16x32_bf16 v[130:133], v[162:165], v[234:237], v[130:133]
	s_waitcnt vmcnt(11)
	s_add_u32 s88, s87, 0x1b8000
	v_cvt_pk_bf16_f32 v6, v6, v7
	v_mfma_f32_16x16x32_bf16 v[134:137], v[166:169], v[234:237], v[134:137]
	v_cvt_pk_bf16_f32 v7, v8, v9
	ds_write_b64 v242, v[6:7] offset:16640
	s_addc_u32 s89, s90, 0
	v_mfma_f32_16x16x32_bf16 v[138:141], v[250:253], v[234:237], v[138:141]
	global_load_dwordx4 v[6:9], v199, s[88:89] nt
	v_mfma_f32_16x16x32_bf16 v[142:145], v[226:229], v[234:237], v[142:145]
	s_waitcnt lgkmcnt(2)
	v_mfma_f32_16x16x32_bf16 v[146:149], v[162:165], v[222:225], v[146:149]
	s_waitcnt vmcnt(11)
	s_add_u32 s88, s87, 0x1e4000
	v_cvt_pk_bf16_f32 v2, v2, v3
	v_mfma_f32_16x16x32_bf16 v[150:153], v[166:169], v[222:225], v[150:153]
	v_cvt_pk_bf16_f32 v3, v4, v5
	ds_write_b64 v242, v[2:3] offset:24832
	s_addc_u32 s89, s90, 0
	v_mfma_f32_16x16x32_bf16 v[154:157], v[250:253], v[222:225], v[154:157]
	global_load_dwordx4 v[2:5], v199, s[88:89] nt
	v_mfma_f32_16x16x32_bf16 v[158:161], v[226:229], v[222:225], v[158:161]
	s_add_i32 s87, s86, 0x8000
	s_cmp_lg_u32 s86, 0x10000
	s_cselect_b32 s86, s87, 0
	s_add_i32 s87, s85, 0x8000
	s_cmp_lg_u32 s85, 0x10000
	s_cselect_b32 s85, s87, 0
	s_add_u32 s2, s2, 0xb0000
	s_addc_u32 s3, s3, 0
	s_add_i32 s39, s39, 0x8000
	v_add_u32_e32 v218, 0x80, v218
	v_add_u32_e32 v219, 0x80, v219
	v_add_u32_e32 v220, 0x80, v220
	v_add_u32_e32 v221, 0x80, v221
	s_add_i32 s88, s39, 0xffff8000
	s_and_b32 s88, s88, 0x8000
	s_add_i32 s88, s88, 0
	s_add_i32 s87, s86, 0
	s_add_i32 s88, s88, 0x18000
	v_add_u32_e32 v246, s88, v212
	v_add_u32_e32 v247, s87, v215
	v_add_u32_e32 v252, s88, v181
	v_add_u32_e32 v254, s88, v172
	v_add_u32_e32 v250, s88, v183
	s_waitcnt lgkmcnt(0)
	s_barrier
	s_cmp_lg_u32 s2, 0x14a0000
	s_cbranch_scc1 .Lrot_m1
	v_add_u32_e32 v200, s52, v212
	v_add_u32_e32 v250, 0, v215
	v_add_u32_e32 v215, s52, v181
	v_add_u32_e32 v251, s52, v172
	v_add_u32_e32 v217, s52, v183
	ds_read_b64_tr_b16 v[162:163], v200
	ds_read_b64_tr_b16 v[164:165], v200 offset:2048
	ds_read_b64_tr_b16 v[166:167], v217
	ds_read_b64_tr_b16 v[168:169], v217 offset:2048
	ds_read_b128 v[218:221], v250
	ds_read_b128 v[222:225], v250 offset:2048
	ds_read_b64_tr_b16 v[226:227], v215
	ds_read_b64_tr_b16 v[228:229], v215 offset:2048
	ds_read_b64_tr_b16 v[230:231], v251
	ds_read_b64_tr_b16 v[232:233], v251 offset:2048
	s_waitcnt lgkmcnt(5)
	v_mfma_f32_16x16x32_bf16 v[62:65], v[162:165], v[218:221], v[62:65]
	ds_read_b128 v[234:237], v250 offset:4096
	v_mfma_f32_16x16x32_bf16 v[58:61], v[166:169], v[218:221], v[58:61]
	s_waitcnt lgkmcnt(3)
	v_mfma_f32_16x16x32_bf16 v[54:57], v[226:229], v[218:221], v[54:57]
	s_waitcnt lgkmcnt(1)
	v_mfma_f32_16x16x32_bf16 v[42:45], v[230:233], v[218:221], v[42:45]
	v_mfma_f32_16x16x32_bf16 v[50:53], v[162:165], v[222:225], v[50:53]
	ds_read_b128 v[218:221], v250 offset:6144
	v_mfma_f32_16x16x32_bf16 v[46:49], v[166:169], v[222:225], v[46:49]
	v_mfma_f32_16x16x32_bf16 v[38:41], v[226:229], v[222:225], v[38:41]
	v_mfma_f32_16x16x32_bf16 v[34:37], v[230:233], v[222:225], v[34:37]
	s_waitcnt lgkmcnt(1)
	v_mfma_f32_16x16x32_bf16 v[66:69], v[162:165], v[234:237], v[66:69]
	ds_read_b128 v[222:225], v250 offset:8192
	v_mfma_f32_16x16x32_bf16 v[70:73], v[166:169], v[234:237], v[70:73]
	v_mfma_f32_16x16x32_bf16 v[74:77], v[226:229], v[234:237], v[74:77]
	v_mfma_f32_16x16x32_bf16 v[78:81], v[230:233], v[234:237], v[78:81]
	s_waitcnt lgkmcnt(1)
	v_mfma_f32_16x16x32_bf16 v[82:85], v[162:165], v[218:221], v[82:85]
	ds_read_b128 v[234:237], v250 offset:10240
	v_mfma_f32_16x16x32_bf16 v[86:89], v[166:169], v[218:221], v[86:89]
	v_mfma_f32_16x16x32_bf16 v[90:93], v[226:229], v[218:221], v[90:93]
	v_mfma_f32_16x16x32_bf16 v[94:97], v[230:233], v[218:221], v[94:97]
	ds_read_b128 v[218:221], v250 offset:12288
	ds_read_b64_tr_b16 v[238:239], v200 offset:16384
	ds_read_b64_tr_b16 v[240:241], v200 offset:18432
	s_waitcnt lgkmcnt(4)
	v_mfma_f32_16x16x32_bf16 v[98:101], v[162:165], v[222:225], v[98:101]
	v_mfma_f32_16x16x32_bf16 v[102:105], v[166:169], v[222:225], v[102:105]
	v_mfma_f32_16x16x32_bf16 v[106:109], v[226:229], v[222:225], v[106:109]
	v_mfma_f32_16x16x32_bf16 v[110:113], v[230:233], v[222:225], v[110:113]
	ds_read_b128 v[222:225], v250 offset:14336
	ds_read_b64_tr_b16 v[242:243], v217 offset:16384
	ds_read_b64_tr_b16 v[244:245], v217 offset:18432
	s_waitcnt lgkmcnt(6)
	v_mfma_f32_16x16x32_bf16 v[114:117], v[162:165], v[234:237], v[114:117]
	v_mfma_f32_16x16x32_bf16 v[118:121], v[166:169], v[234:237], v[118:121]
	v_mfma_f32_16x16x32_bf16 v[122:125], v[226:229], v[234:237], v[122:125]
	v_mfma_f32_16x16x32_bf16 v[126:129], v[230:233], v[234:237], v[126:129]
	v_add_u32_e32 v200, 0, v216
	ds_read_b128 v[234:237], v200
	ds_read_b64_tr_b16 v[246:247], v215 offset:16384
	ds_read_b64_tr_b16 v[248:249], v215 offset:18432
	s_waitcnt lgkmcnt(8)
	v_mfma_f32_16x16x32_bf16 v[130:133], v[162:165], v[218:221], v[130:133]
	v_mfma_f32_16x16x32_bf16 v[134:137], v[166:169], v[218:221], v[134:137]
	v_mfma_f32_16x16x32_bf16 v[138:141], v[226:229], v[218:221], v[138:141]
	v_mfma_f32_16x16x32_bf16 v[142:145], v[230:233], v[218:221], v[142:145]
	s_waitcnt lgkmcnt(5)
	v_mfma_f32_16x16x32_bf16 v[146:149], v[162:165], v[222:225], v[146:149]
	v_mfma_f32_16x16x32_bf16 v[150:153], v[166:169], v[222:225], v[150:153]
	ds_read_b128 v[162:165], v200 offset:2048
	ds_read_b64_tr_b16 v[166:167], v251 offset:16384
	ds_read_b64_tr_b16 v[168:169], v251 offset:18432
	v_mfma_f32_16x16x32_bf16 v[154:157], v[226:229], v[222:225], v[154:157]
	v_mfma_f32_16x16x32_bf16 v[158:161], v[230:233], v[222:225], v[158:161]
	ds_read_b128 v[216:219], v200 offset:4096
	s_waitcnt vmcnt(7)
	v_add_u32_e32 v214, s56, v214
	v_cvt_pk_bf16_f32 v30, v30, v31
	v_cvt_pk_bf16_f32 v31, v32, v33
	s_waitcnt lgkmcnt(6)
	v_mfma_f32_16x16x32_bf16 v[62:65], v[238:241], v[234:237], v[62:65]
	ds_write_b64 v214, v[30:31]
	v_mfma_f32_16x16x32_bf16 v[58:61], v[242:245], v[234:237], v[58:61]
	s_waitcnt lgkmcnt(5)
	v_mfma_f32_16x16x32_bf16 v[54:57], v[246:249], v[234:237], v[54:57]
	s_waitcnt lgkmcnt(2)
	v_mfma_f32_16x16x32_bf16 v[30:33], v[166:169], v[234:237], v[42:45]
	v_mfma_f32_16x16x32_bf16 v[42:45], v[238:241], v[162:165], v[50:53]
	s_nop 2
	ds_read_b128 v[50:53], v200 offset:6144
	s_waitcnt vmcnt(6)
	v_mfma_f32_16x16x32_bf16 v[46:49], v[242:245], v[162:165], v[46:49]
	v_cvt_pk_bf16_f32 v26, v26, v27
	v_cvt_pk_bf16_f32 v27, v28, v29
	ds_write_b64 v214, v[26:27] offset:8192
	v_mfma_f32_16x16x32_bf16 v[38:41], v[246:249], v[162:165], v[38:41]
	v_mfma_f32_16x16x32_bf16 v[26:29], v[166:169], v[162:165], v[34:37]
	s_waitcnt lgkmcnt(3)
	v_mfma_f32_16x16x32_bf16 v[34:37], v[238:241], v[216:219], v[66:69]
	v_mfma_f32_16x16x32_bf16 v[66:69], v[242:245], v[216:219], v[70:73]
	s_nop 2
	ds_read_b128 v[70:73], v200 offset:8192
	s_waitcnt vmcnt(5)
	v_mfma_f32_16x16x32_bf16 v[74:77], v[246:249], v[216:219], v[74:77]
	v_cvt_pk_bf16_f32 v22, v22, v23
	v_cvt_pk_bf16_f32 v23, v24, v25
	ds_write_b64 v214, v[22:23] offset:16384
	v_mfma_f32_16x16x32_bf16 v[22:25], v[166:169], v[216:219], v[78:81]
	s_waitcnt lgkmcnt(3)
	v_mfma_f32_16x16x32_bf16 v[78:81], v[238:241], v[50:53], v[82:85]
	v_mfma_f32_16x16x32_bf16 v[82:85], v[242:245], v[50:53], v[86:89]
	s_nop 2
	ds_read_b128 v[86:89], v200 offset:10240
	s_waitcnt vmcnt(4)
	v_mfma_f32_16x16x32_bf16 v[90:93], v[246:249], v[50:53], v[90:93]
	v_cvt_pk_bf16_f32 v18, v18, v19
	v_cvt_pk_bf16_f32 v19, v20, v21
	ds_write_b64 v214, v[18:19] offset:24576
	v_mfma_f32_16x16x32_bf16 v[18:21], v[166:169], v[50:53], v[94:97]
	s_waitcnt lgkmcnt(3)
	v_mfma_f32_16x16x32_bf16 v[50:53], v[238:241], v[70:73], v[98:101]
	v_add_u32_e32 v162, s56, v213
	s_nop 1
	ds_read_b128 v[98:101], v200 offset:12288
	s_waitcnt vmcnt(3)
	v_mfma_f32_16x16x32_bf16 v[94:97], v[242:245], v[70:73], v[102:105]
	v_cvt_pk_bf16_f32 v14, v14, v15
	v_cvt_pk_bf16_f32 v15, v16, v17
	ds_write_b64 v162, v[14:15]
	v_mfma_f32_16x16x32_bf16 v[102:105], v[246:249], v[70:73], v[106:109]
	v_mfma_f32_16x16x32_bf16 v[14:17], v[166:169], v[70:73], v[110:113]
	s_nop 2
	ds_read_b128 v[110:113], v200 offset:14336
	s_waitcnt vmcnt(2)
	s_waitcnt lgkmcnt(4)
	v_mfma_f32_16x16x32_bf16 v[70:73], v[238:241], v[86:89], v[114:117]
	v_cvt_pk_bf16_f32 v10, v10, v11
	v_cvt_pk_bf16_f32 v11, v12, v13
	ds_write_b64 v162, v[10:11] offset:8192
	v_mfma_f32_16x16x32_bf16 v[106:109], v[242:245], v[86:89], v[118:121]
	v_mfma_f32_16x16x32_bf16 v[114:117], v[246:249], v[86:89], v[122:125]
	v_mfma_f32_16x16x32_bf16 v[10:13], v[166:169], v[86:89], v[126:129]
	s_waitcnt vmcnt(1)
	s_waitcnt lgkmcnt(3)
	v_mfma_f32_16x16x32_bf16 v[86:89], v[238:241], v[98:101], v[130:133]
	v_cvt_pk_bf16_f32 v6, v6, v7
	v_cvt_pk_bf16_f32 v7, v8, v9
	ds_write_b64 v162, v[6:7] offset:16384
	v_mfma_f32_16x16x32_bf16 v[118:121], v[242:245], v[98:101], v[134:137]
	v_mfma_f32_16x16x32_bf16 v[122:125], v[246:249], v[98:101], v[138:141]
	v_mfma_f32_16x16x32_bf16 v[6:9], v[166:169], v[98:101], v[142:145]
	s_waitcnt vmcnt(0)
	s_waitcnt lgkmcnt(2)
	v_mfma_f32_16x16x32_bf16 v[98:101], v[238:241], v[110:113], v[146:149]
	v_cvt_pk_bf16_f32 v2, v2, v3
	v_cvt_pk_bf16_f32 v3, v4, v5
	ds_write_b64 v162, v[2:3] offset:24576
	v_mfma_f32_16x16x32_bf16 v[126:129], v[242:245], v[110:113], v[150:153]
	v_mfma_f32_16x16x32_bf16 v[130:133], v[246:249], v[110:113], v[154:157]
	v_mfma_f32_16x16x32_bf16 v[2:5], v[166:169], v[110:113], v[158:161]
	s_waitcnt lgkmcnt(0)
	s_barrier
	v_add_u32_e32 v168, s56, v212
	v_add_u32_e32 v183, s56, v183
	v_add_u32_e32 v181, s56, v181
	ds_read_b64_tr_b16 v[110:111], v168
	ds_read_b64_tr_b16 v[112:113], v168 offset:2048
	ds_read_b64_tr_b16 v[134:135], v183
	ds_read_b64_tr_b16 v[136:137], v183 offset:2048
	ds_read_b128 v[138:141], v250 offset:32768
	ds_read_b64_tr_b16 v[142:143], v181
	ds_read_b128 v[146:149], v250 offset:34816
	ds_read_b128 v[150:153], v250 offset:36864
	ds_read_b64_tr_b16 v[144:145], v181 offset:2048
	v_add_u32_e32 v172, s56, v172
	ds_read_b64_tr_b16 v[154:155], v172
	ds_read_b64_tr_b16 v[156:157], v172 offset:2048
	s_waitcnt lgkmcnt(6)
	v_mfma_f32_16x16x32_bf16 v[62:65], v[110:113], v[138:141], v[62:65]
	v_mfma_f32_16x16x32_bf16 v[58:61], v[134:137], v[138:141], v[58:61]
	s_waitcnt lgkmcnt(2)
	v_mfma_f32_16x16x32_bf16 v[54:57], v[142:145], v[138:141], v[54:57]
	s_waitcnt lgkmcnt(0)
	v_mfma_f32_16x16x32_bf16 v[30:33], v[154:157], v[138:141], v[30:33]
	v_mfma_f32_16x16x32_bf16 v[42:45], v[110:113], v[146:149], v[42:45]
	ds_read_b128 v[138:141], v250 offset:38912
	v_mfma_f32_16x16x32_bf16 v[46:49], v[134:137], v[146:149], v[46:49]
	v_mfma_f32_16x16x32_bf16 v[38:41], v[142:145], v[146:149], v[38:41]
	v_mfma_f32_16x16x32_bf16 v[26:29], v[154:157], v[146:149], v[26:29]
	v_mfma_f32_16x16x32_bf16 v[34:37], v[110:113], v[150:153], v[34:37]
	ds_read_b128 v[146:149], v250 offset:40960
	v_mfma_f32_16x16x32_bf16 v[66:69], v[134:137], v[150:153], v[66:69]
	v_mfma_f32_16x16x32_bf16 v[74:77], v[142:145], v[150:153], v[74:77]
	v_mfma_f32_16x16x32_bf16 v[22:25], v[154:157], v[150:153], v[22:25]
	s_waitcnt lgkmcnt(1)
	v_mfma_f32_16x16x32_bf16 v[150:153], v[134:137], v[138:141], v[82:85]
	s_nop 2
	ds_read_b128 v[82:85], v250 offset:43008
	v_mfma_f32_16x16x32_bf16 v[78:81], v[110:113], v[138:141], v[78:81]
	v_mfma_f32_16x16x32_bf16 v[18:21], v[154:157], v[138:141], v[18:21]
	v_mfma_f32_16x16x32_bf16 v[158:161], v[142:145], v[138:141], v[90:93]
	s_nop 2
	ds_read_b128 v[90:93], v250 offset:45056
	ds_read_b64_tr_b16 v[166:167], v168 offset:16384
	ds_read_b64_tr_b16 v[168:169], v168 offset:18432
	s_waitcnt lgkmcnt(4)
	v_mfma_f32_16x16x32_bf16 v[50:53], v[110:113], v[146:149], v[50:53]
	v_mfma_f32_16x16x32_bf16 v[14:17], v[154:157], v[146:149], v[14:17]
	v_mfma_f32_16x16x32_bf16 v[138:141], v[134:137], v[146:149], v[94:97]
	v_mfma_f32_16x16x32_bf16 v[162:165], v[142:145], v[146:149], v[102:105]
	s_waitcnt lgkmcnt(3)
	v_mfma_f32_16x16x32_bf16 v[146:149], v[110:113], v[82:85], v[70:73]
	s_nop 2
	ds_read_b128 v[70:73], v250 offset:47104
	ds_read_b64_tr_b16 v[220:221], v183 offset:16384
	ds_read_b64_tr_b16 v[222:223], v183 offset:18432
	v_mfma_f32_16x16x32_bf16 v[10:13], v[154:157], v[82:85], v[10:13]
	v_mfma_f32_16x16x32_bf16 v[212:215], v[134:137], v[82:85], v[106:109]
	v_mfma_f32_16x16x32_bf16 v[216:219], v[142:145], v[82:85], v[114:117]
	ds_read_b128 v[82:85], v200 offset:32768
	ds_read_b64_tr_b16 v[236:237], v181 offset:16384
	ds_read_b64_tr_b16 v[238:239], v181 offset:18432
	s_waitcnt lgkmcnt(8)
	v_mfma_f32_16x16x32_bf16 v[6:9], v[154:157], v[90:93], v[6:9]
	v_mfma_f32_16x16x32_bf16 v[224:227], v[110:113], v[90:93], v[86:89]
	v_mfma_f32_16x16x32_bf16 v[228:231], v[134:137], v[90:93], v[118:121]
	v_mfma_f32_16x16x32_bf16 v[232:235], v[142:145], v[90:93], v[122:125]
	s_waitcnt lgkmcnt(5)
	v_mfma_f32_16x16x32_bf16 v[130:133], v[142:145], v[70:73], v[130:133]
	ds_read_b128 v[86:89], v200 offset:34816
	ds_read_b64_tr_b16 v[142:143], v172 offset:16384
	ds_read_b64_tr_b16 v[144:145], v172 offset:18432
	v_mfma_f32_16x16x32_bf16 v[240:243], v[110:113], v[70:73], v[98:101]
	v_mfma_f32_16x16x32_bf16 v[134:137], v[134:137], v[70:73], v[126:129]
	v_mfma_f32_16x16x32_bf16 v[154:157], v[154:157], v[70:73], v[2:5]
	s_nop 2
	ds_read_b128 v[2:5], v200 offset:36864
	s_waitcnt lgkmcnt(6)
	v_mfma_f32_16x16x32_bf16 v[122:125], v[166:169], v[82:85], v[62:65]
	v_mfma_f32_16x16x32_bf16 v[114:117], v[220:223], v[82:85], v[58:61]
	s_waitcnt lgkmcnt(4)
	v_mfma_f32_16x16x32_bf16 v[126:129], v[236:239], v[82:85], v[54:57]
	s_waitcnt lgkmcnt(1)
	v_mfma_f32_16x16x32_bf16 v[118:121], v[142:145], v[82:85], v[30:33]
	s_nop 2
	ds_read_b128 v[30:33], v200 offset:38912
	v_mfma_f32_16x16x32_bf16 v[106:109], v[166:169], v[86:89], v[42:45]
	v_mfma_f32_16x16x32_bf16 v[98:101], v[220:223], v[86:89], v[46:49]
	v_mfma_f32_16x16x32_bf16 v[110:113], v[236:239], v[86:89], v[38:41]
	v_mfma_f32_16x16x32_bf16 v[102:105], v[142:145], v[86:89], v[26:29]
	s_nop 2
	ds_read_b128 v[26:29], v200 offset:40960
	s_waitcnt lgkmcnt(2)
	v_mfma_f32_16x16x32_bf16 v[90:93], v[166:169], v[2:5], v[34:37]
	v_mfma_f32_16x16x32_bf16 v[82:85], v[220:223], v[2:5], v[66:69]
	v_mfma_f32_16x16x32_bf16 v[94:97], v[236:239], v[2:5], v[74:77]
	v_mfma_f32_16x16x32_bf16 v[86:89], v[142:145], v[2:5], v[22:25]
	ds_read_b128 v[2:5], v200 offset:43008
	s_waitcnt lgkmcnt(2)
	v_mfma_f32_16x16x32_bf16 v[74:77], v[166:169], v[30:33], v[78:81]
	v_mfma_f32_16x16x32_bf16 v[66:69], v[220:223], v[30:33], v[150:153]
	v_mfma_f32_16x16x32_bf16 v[78:81], v[236:239], v[30:33], v[158:161]
	v_mfma_f32_16x16x32_bf16 v[70:73], v[142:145], v[30:33], v[18:21]
	ds_read_b128 v[22:25], v200 offset:45056
	s_waitcnt lgkmcnt(2)
	v_mfma_f32_16x16x32_bf16 v[58:61], v[166:169], v[26:29], v[50:53]
	v_mfma_f32_16x16x32_bf16 v[50:53], v[220:223], v[26:29], v[138:141]
	v_mfma_f32_16x16x32_bf16 v[62:65], v[236:239], v[26:29], v[162:165]
	v_mfma_f32_16x16x32_bf16 v[54:57], v[142:145], v[26:29], v[14:17]
	s_waitcnt lgkmcnt(1)
	v_mfma_f32_16x16x32_bf16 v[42:45], v[166:169], v[2:5], v[146:149]
	ds_read_b128 v[138:141], v200 offset:47104
	v_mfma_f32_16x16x32_bf16 v[34:37], v[220:223], v[2:5], v[212:215]
	v_mfma_f32_16x16x32_bf16 v[46:49], v[236:239], v[2:5], v[216:219]
	v_mfma_f32_16x16x32_bf16 v[38:41], v[142:145], v[2:5], v[10:13]
	s_waitcnt lgkmcnt(1)
	v_mfma_f32_16x16x32_bf16 v[26:29], v[166:169], v[22:25], v[224:227]
	v_mfma_f32_16x16x32_bf16 v[18:21], v[220:223], v[22:25], v[228:231]
	v_mfma_f32_16x16x32_bf16 v[30:33], v[236:239], v[22:25], v[232:235]
	v_mfma_f32_16x16x32_bf16 v[22:25], v[142:145], v[22:25], v[6:9]
	s_waitcnt lgkmcnt(0)
	v_mfma_f32_16x16x32_bf16 v[10:13], v[166:169], v[138:141], v[240:243]
	v_mfma_f32_16x16x32_bf16 v[2:5], v[220:223], v[138:141], v[134:137]
	v_mfma_f32_16x16x32_bf16 v[14:17], v[236:239], v[138:141], v[130:133]
	v_mfma_f32_16x16x32_bf16 v[6:9], v[142:145], v[138:141], v[154:157]
	s_waitcnt lgkmcnt(0)
	s_barrier
	s_nop 0
	v_mov_b32_e32 v130, 0
	s_and_b64 vcc, exec, s[6:7]
	v_mov_b32_e32 v131, 0
	v_mov_b32_e32 v132, 0
	s_cbranch_vccnz .LBB0_1436
	global_load_dword v130, v[184:185], off
	global_load_dword v131, v[186:187], off
	global_load_dword v132, v[188:189], off

.Lrot_m2:
	ds_read_b64_tr_b16 v[210:211], v234
	ds_read_b64_tr_b16 v[212:213], v234 offset:2048
	ds_read_b64_tr_b16 v[214:215], v238
	ds_read_b64_tr_b16 v[216:217], v238 offset:2048
	ds_read_b128 v[162:165], v235
	ds_read_b128 v[166:169], v235 offset:2048
	ds_read_b64_tr_b16 v[218:219], v240
	ds_read_b64_tr_b16 v[220:221], v240 offset:2048
	ds_read_b64_tr_b16 v[222:223], v242
	ds_read_b64_tr_b16 v[224:225], v242 offset:2048
	s_waitcnt lgkmcnt(5)
	v_mfma_f32_16x16x32_bf16 v[34:37], v[210:213], v[162:165], v[34:37]
	ds_read_b128 v[226:229], v235 offset:4096
	s_and_b32 s42, s37, 0x8000
	v_add_u32_e32 v230, 0xffef8000, v209
	v_mfma_f32_16x16x32_bf16 v[38:41], v[214:217], v[162:165], v[38:41]
	s_add_i32 s43, s36, s39
	s_mov_b32 s44, m0
	s_mov_b32 m0, s43
	s_nop 0
	global_load_lds_dwordx4 v230, s[14:15]
	s_mov_b32 m0, s44
	s_waitcnt lgkmcnt(3)
	v_mfma_f32_16x16x32_bf16 v[42:45], v[218:221], v[162:165], v[42:45]
	s_waitcnt lgkmcnt(1)
	v_mfma_f32_16x16x32_bf16 v[46:49], v[222:225], v[162:165], v[46:49]
	v_mfma_f32_16x16x32_bf16 v[50:53], v[210:213], v[166:169], v[50:53]
	ds_read_b128 v[162:165], v235 offset:6144
	v_add_u32_e32 v230, 0xfff50000, v209
	s_add_i32 s44, s43, 0x2000
	v_mfma_f32_16x16x32_bf16 v[54:57], v[214:217], v[166:169], v[54:57]
	s_mov_b32 s45, m0
	s_mov_b32 m0, s44
	s_nop 0
	global_load_lds_dwordx4 v230, s[14:15]
	s_mov_b32 m0, s45
	v_mfma_f32_16x16x32_bf16 v[58:61], v[218:221], v[166:169], v[58:61]
	v_mfma_f32_16x16x32_bf16 v[62:65], v[222:225], v[166:169], v[62:65]
	s_waitcnt lgkmcnt(1)
	v_mfma_f32_16x16x32_bf16 v[66:69], v[210:213], v[226:229], v[66:69]
	ds_read_b128 v[166:169], v235 offset:8192
	v_add_u32_e32 v230, 0xfffa8000, v209
	s_add_i32 s44, s43, 0x4000
	v_mfma_f32_16x16x32_bf16 v[70:73], v[214:217], v[226:229], v[70:73]
	s_mov_b32 s45, m0
	s_mov_b32 m0, s44
	s_nop 0
	global_load_lds_dwordx4 v230, s[14:15]
	s_mov_b32 m0, s45
	v_mfma_f32_16x16x32_bf16 v[74:77], v[218:221], v[226:229], v[74:77]
	v_mfma_f32_16x16x32_bf16 v[78:81], v[222:225], v[226:229], v[78:81]
	s_waitcnt lgkmcnt(1)
	v_mfma_f32_16x16x32_bf16 v[82:85], v[210:213], v[162:165], v[82:85]
	ds_read_b128 v[226:229], v235 offset:10240
	s_addk_i32 s43, 0x6000
	s_mov_b32 s44, m0
	s_mov_b32 m0, s43
	s_nop 0
	global_load_lds_dwordx4 v209, s[14:15]
	s_mov_b32 m0, s44
	v_mfma_f32_16x16x32_bf16 v[86:89], v[214:217], v[162:165], v[86:89]
	v_mfma_f32_16x16x32_bf16 v[90:93], v[218:221], v[162:165], v[90:93]
	v_mfma_f32_16x16x32_bf16 v[94:97], v[222:225], v[162:165], v[94:97]
	ds_read_b128 v[230:233], v235 offset:12288
	ds_read_b64_tr_b16 v[162:163], v234 offset:16384
	ds_read_b64_tr_b16 v[164:165], v234 offset:18432
	s_waitcnt lgkmcnt(4)
	v_mfma_f32_16x16x32_bf16 v[98:101], v[210:213], v[166:169], v[98:101]
	v_mfma_f32_16x16x32_bf16 v[102:105], v[214:217], v[166:169], v[102:105]
	v_mfma_f32_16x16x32_bf16 v[106:109], v[218:221], v[166:169], v[106:109]
	v_mfma_f32_16x16x32_bf16 v[110:113], v[222:225], v[166:169], v[110:113]
	ds_read_b128 v[234:237], v235 offset:14336
	ds_read_b64_tr_b16 v[166:167], v238 offset:16384
	ds_read_b64_tr_b16 v[168:169], v238 offset:18432
	s_waitcnt lgkmcnt(6)
	v_mfma_f32_16x16x32_bf16 v[114:117], v[210:213], v[226:229], v[114:117]
	v_mfma_f32_16x16x32_bf16 v[118:121], v[214:217], v[226:229], v[118:121]
	v_mfma_f32_16x16x32_bf16 v[122:125], v[218:221], v[226:229], v[122:125]
	v_mfma_f32_16x16x32_bf16 v[126:129], v[222:225], v[226:229], v[126:129]
	v_add_u32_e32 v243, s41, v208
	ds_read_b128 v[226:229], v243
	ds_read_b64_tr_b16 v[238:239], v240 offset:16384
	ds_read_b64_tr_b16 v[240:241], v240 offset:18432
	s_waitcnt lgkmcnt(8)
	v_mfma_f32_16x16x32_bf16 v[130:133], v[210:213], v[230:233], v[130:133]
	v_mfma_f32_16x16x32_bf16 v[134:137], v[214:217], v[230:233], v[134:137]
	v_mfma_f32_16x16x32_bf16 v[138:141], v[218:221], v[230:233], v[138:141]
	v_mfma_f32_16x16x32_bf16 v[142:145], v[222:225], v[230:233], v[142:145]
	s_waitcnt lgkmcnt(5)
	v_mfma_f32_16x16x32_bf16 v[146:149], v[210:213], v[234:237], v[146:149]
	ds_read_b128 v[210:213], v243 offset:2048
	s_add_i32 s41, s24, s42
	v_mfma_f32_16x16x32_bf16 v[150:153], v[214:217], v[234:237], v[150:153]
	ds_read_b64_tr_b16 v[214:215], v242 offset:16384
	ds_read_b64_tr_b16 v[216:217], v242 offset:18432
	v_mfma_f32_16x16x32_bf16 v[158:161], v[218:221], v[234:237], v[158:161]
	v_mfma_f32_16x16x32_bf16 v[154:157], v[222:225], v[234:237], v[154:157]
	ds_read_b128 v[218:221], v243 offset:4096
	s_waitcnt lgkmcnt(6)
	v_mfma_f32_16x16x32_bf16 v[34:37], v[162:165], v[226:229], v[34:37]
	s_add_u32 s44, s2, s16
	s_waitcnt vmcnt(11)
	s_addc_u32 s45, s38, s17
	v_mfma_f32_16x16x32_bf16 v[38:41], v[166:169], v[226:229], v[38:41]
	v_cvt_pk_bf16_f32 v30, v30, v31
	v_cvt_pk_bf16_f32 v31, v32, v33
	v_add_u32_e32 v230, s41, v206
	s_waitcnt lgkmcnt(4)
	v_mfma_f32_16x16x32_bf16 v[42:45], v[238:241], v[226:229], v[42:45]
	s_add_u32 s42, s44, 0x100000
	ds_write_b64 v230, v[30:31]
	s_addc_u32 s43, s45, 0
	s_waitcnt lgkmcnt(2)
	v_mfma_f32_16x16x32_bf16 v[46:49], v[214:217], v[226:229], v[46:49]
	global_load_dwordx4 v[30:33], v199, s[42:43] nt
	v_mfma_f32_16x16x32_bf16 v[50:53], v[162:165], v[210:213], v[50:53]
	ds_read_b128 v[222:225], v243 offset:6144
	s_waitcnt vmcnt(11)
	v_add_u32_e32 v226, s41, v205
	v_mfma_f32_16x16x32_bf16 v[54:57], v[166:169], v[210:213], v[54:57]
	v_cvt_pk_bf16_f32 v26, v26, v27
	v_cvt_pk_bf16_f32 v27, v28, v29
	s_add_u32 s42, s44, 0x110000
	v_mfma_f32_16x16x32_bf16 v[58:61], v[238:241], v[210:213], v[58:61]
	ds_write_b64 v226, v[26:27] offset:4096
	s_addc_u32 s43, s45, 0
	global_load_dwordx4 v[26:29], v199, s[42:43] nt
	v_mfma_f32_16x16x32_bf16 v[62:65], v[214:217], v[210:213], v[62:65]
	s_waitcnt lgkmcnt(3)
	v_mfma_f32_16x16x32_bf16 v[66:69], v[162:165], v[218:221], v[66:69]
	ds_read_b128 v[210:213], v243 offset:8192
	s_waitcnt vmcnt(11)
	s_add_u32 s42, s44, 0x120000
	v_mfma_f32_16x16x32_bf16 v[70:73], v[166:169], v[218:221], v[70:73]
	v_cvt_pk_bf16_f32 v22, v22, v23
	v_cvt_pk_bf16_f32 v23, v24, v25
	ds_write_b64 v230, v[22:23] offset:8192
	v_mfma_f32_16x16x32_bf16 v[74:77], v[238:241], v[218:221], v[74:77]
	s_addc_u32 s43, s45, 0
	global_load_dwordx4 v[22:25], v199, s[42:43] nt
	v_mfma_f32_16x16x32_bf16 v[78:81], v[214:217], v[218:221], v[78:81]
	s_waitcnt lgkmcnt(3)
	v_mfma_f32_16x16x32_bf16 v[82:85], v[162:165], v[222:225], v[82:85]
	ds_read_b128 v[218:221], v243 offset:10240
	s_waitcnt vmcnt(11)
	s_add_u32 s42, s44, 0x130000
	v_mfma_f32_16x16x32_bf16 v[86:89], v[166:169], v[222:225], v[86:89]
	v_cvt_pk_bf16_f32 v18, v18, v19
	v_cvt_pk_bf16_f32 v19, v20, v21
	ds_write_b64 v226, v[18:19] offset:12288
	v_mfma_f32_16x16x32_bf16 v[90:93], v[238:241], v[222:225], v[90:93]
	s_addc_u32 s43, s45, 0
	global_load_dwordx4 v[18:21], v199, s[42:43] nt
	v_mfma_f32_16x16x32_bf16 v[94:97], v[214:217], v[222:225], v[94:97]
	s_waitcnt lgkmcnt(3)
	v_mfma_f32_16x16x32_bf16 v[98:101], v[162:165], v[210:213], v[98:101]
	ds_read_b128 v[222:225], v243 offset:12288
	s_waitcnt vmcnt(11)
	s_add_u32 s42, s44, 0x140000
	v_mfma_f32_16x16x32_bf16 v[102:105], v[166:169], v[210:213], v[102:105]
	v_cvt_pk_bf16_f32 v14, v14, v15
	v_cvt_pk_bf16_f32 v15, v16, v17
	ds_write_b64 v230, v[14:15] offset:16384
	v_mfma_f32_16x16x32_bf16 v[106:109], v[238:241], v[210:213], v[106:109]
	s_addc_u32 s43, s45, 0
	global_load_dwordx4 v[14:17], v199, s[42:43] nt
	v_mfma_f32_16x16x32_bf16 v[110:113], v[214:217], v[210:213], v[110:113]
	s_waitcnt lgkmcnt(3)
	v_mfma_f32_16x16x32_bf16 v[114:117], v[162:165], v[218:221], v[114:117]
	ds_read_b128 v[210:213], v243 offset:14336
	s_waitcnt vmcnt(11)
	s_add_u32 s42, s44, 0x150000
	v_mfma_f32_16x16x32_bf16 v[118:121], v[166:169], v[218:221], v[118:121]
	v_cvt_pk_bf16_f32 v10, v10, v11
	v_cvt_pk_bf16_f32 v11, v12, v13
	ds_write_b64 v226, v[10:11] offset:20480
	v_mfma_f32_16x16x32_bf16 v[122:125], v[238:241], v[218:221], v[122:125]
	s_addc_u32 s43, s45, 0
	global_load_dwordx4 v[10:13], v199, s[42:43] nt
	v_mfma_f32_16x16x32_bf16 v[126:129], v[214:217], v[218:221], v[126:129]
	s_waitcnt lgkmcnt(3)
	v_mfma_f32_16x16x32_bf16 v[130:133], v[162:165], v[222:225], v[130:133]
	s_waitcnt vmcnt(11)
	s_add_u32 s42, s44, 0x160000
	v_cvt_pk_bf16_f32 v6, v6, v7
	v_mfma_f32_16x16x32_bf16 v[134:137], v[166:169], v[222:225], v[134:137]
	v_cvt_pk_bf16_f32 v7, v8, v9
	ds_write_b64 v230, v[6:7] offset:24576
	s_addc_u32 s43, s45, 0
	v_mfma_f32_16x16x32_bf16 v[138:141], v[238:241], v[222:225], v[138:141]
	global_load_dwordx4 v[6:9], v199, s[42:43] nt
	v_mfma_f32_16x16x32_bf16 v[142:145], v[214:217], v[222:225], v[142:145]
	s_waitcnt lgkmcnt(2)
	v_mfma_f32_16x16x32_bf16 v[146:149], v[162:165], v[210:213], v[146:149]
	s_waitcnt vmcnt(11)
	s_add_u32 s42, s44, 0x170000
	v_cvt_pk_bf16_f32 v2, v2, v3
	v_mfma_f32_16x16x32_bf16 v[150:153], v[166:169], v[210:213], v[150:153]
	v_cvt_pk_bf16_f32 v3, v4, v5
	ds_write_b64 v226, v[2:3] offset:28672
	s_addc_u32 s43, s45, 0
	v_mfma_f32_16x16x32_bf16 v[158:161], v[238:241], v[210:213], v[158:161]
	global_load_dwordx4 v[2:5], v199, s[42:43] nt
	v_mfma_f32_16x16x32_bf16 v[154:157], v[214:217], v[210:213], v[154:157]
	s_add_i32 s41, s40, 0x8000
	s_cmp_lg_u32 s40, 0x10000
	s_cselect_b32 s40, s41, 0
	s_add_i32 s41, s39, 0x8000
	s_cmp_lg_u32 s39, 0x10000
	s_cselect_b32 s39, s41, 0
	s_add_u32 s16, s16, 0x80000
	s_addc_u32 s17, s17, 0
	s_add_i32 s37, s37, 0x8000
	v_add_u32_e32 v209, 0x80, v209
	s_add_i32 s42, s37, 0xffff8000
	s_and_b32 s42, s42, 0x8000
	s_add_i32 s41, s40, 0
	s_add_i32 s42, s24, s42
	v_add_u32_e32 v234, s42, v183
	v_add_u32_e32 v235, s41, v207
	v_add_u32_e32 v240, s42, v179
	v_add_u32_e32 v242, s42, v172
	v_add_u32_e32 v238, s42, v181
	s_waitcnt lgkmcnt(0)
	s_barrier
	s_cmp_lg_u32 s16, 0x1500000
	s_cbranch_scc1 .Lrot_m2
	v_add_u32_e32 v209, s24, v183
	v_add_u32_e32 v242, 0, v207
	v_add_u32_e32 v207, s24, v179
	v_add_u32_e32 v243, s24, v172
	v_add_u32_e32 v236, s24, v181
	ds_read_b64_tr_b16 v[162:163], v209
	ds_read_b64_tr_b16 v[164:165], v209 offset:2048
	ds_read_b64_tr_b16 v[166:167], v236
	ds_read_b64_tr_b16 v[168:169], v236 offset:2048
	ds_read_b128 v[210:213], v242
	ds_read_b128 v[214:217], v242 offset:2048
	ds_read_b64_tr_b16 v[218:219], v207
	ds_read_b64_tr_b16 v[220:221], v207 offset:2048
	ds_read_b64_tr_b16 v[222:223], v243
	ds_read_b64_tr_b16 v[224:225], v243 offset:2048
	s_waitcnt lgkmcnt(5)
	v_mfma_f32_16x16x32_bf16 v[34:37], v[162:165], v[210:213], v[34:37]
	ds_read_b128 v[226:229], v242 offset:4096
	v_mfma_f32_16x16x32_bf16 v[38:41], v[166:169], v[210:213], v[38:41]
	s_waitcnt lgkmcnt(3)
	v_mfma_f32_16x16x32_bf16 v[42:45], v[218:221], v[210:213], v[42:45]
	s_waitcnt lgkmcnt(1)
	v_mfma_f32_16x16x32_bf16 v[46:49], v[222:225], v[210:213], v[46:49]
	v_mfma_f32_16x16x32_bf16 v[50:53], v[162:165], v[214:217], v[50:53]
	ds_read_b128 v[210:213], v242 offset:6144
	v_mfma_f32_16x16x32_bf16 v[54:57], v[166:169], v[214:217], v[54:57]
	v_mfma_f32_16x16x32_bf16 v[58:61], v[218:221], v[214:217], v[58:61]
	v_mfma_f32_16x16x32_bf16 v[62:65], v[222:225], v[214:217], v[62:65]
	s_waitcnt lgkmcnt(1)
	v_mfma_f32_16x16x32_bf16 v[66:69], v[162:165], v[226:229], v[66:69]
	ds_read_b128 v[214:217], v242 offset:8192
	v_mfma_f32_16x16x32_bf16 v[70:73], v[166:169], v[226:229], v[70:73]
	v_mfma_f32_16x16x32_bf16 v[74:77], v[218:221], v[226:229], v[74:77]
	v_mfma_f32_16x16x32_bf16 v[78:81], v[222:225], v[226:229], v[78:81]
	s_waitcnt lgkmcnt(1)
	v_mfma_f32_16x16x32_bf16 v[82:85], v[162:165], v[210:213], v[82:85]
	ds_read_b128 v[226:229], v242 offset:10240
	v_mfma_f32_16x16x32_bf16 v[86:89], v[166:169], v[210:213], v[86:89]
	v_mfma_f32_16x16x32_bf16 v[90:93], v[218:221], v[210:213], v[90:93]
	v_mfma_f32_16x16x32_bf16 v[94:97], v[222:225], v[210:213], v[94:97]
	ds_read_b128 v[210:213], v242 offset:12288
	ds_read_b64_tr_b16 v[230:231], v209 offset:16384
	ds_read_b64_tr_b16 v[232:233], v209 offset:18432
	s_waitcnt lgkmcnt(4)
	v_mfma_f32_16x16x32_bf16 v[98:101], v[162:165], v[214:217], v[98:101]
	v_mfma_f32_16x16x32_bf16 v[102:105], v[166:169], v[214:217], v[102:105]
	v_mfma_f32_16x16x32_bf16 v[106:109], v[218:221], v[214:217], v[106:109]
	v_mfma_f32_16x16x32_bf16 v[110:113], v[222:225], v[214:217], v[110:113]
	ds_read_b128 v[214:217], v242 offset:14336
	ds_read_b64_tr_b16 v[234:235], v236 offset:16384
	ds_read_b64_tr_b16 v[236:237], v236 offset:18432
	s_waitcnt lgkmcnt(6)
	v_mfma_f32_16x16x32_bf16 v[114:117], v[162:165], v[226:229], v[114:117]
	v_mfma_f32_16x16x32_bf16 v[118:121], v[166:169], v[226:229], v[118:121]
	v_mfma_f32_16x16x32_bf16 v[122:125], v[218:221], v[226:229], v[122:125]
	v_mfma_f32_16x16x32_bf16 v[126:129], v[222:225], v[226:229], v[126:129]
	v_add_u32_e32 v244, 0, v208
	ds_read_b128 v[226:229], v244
	ds_read_b64_tr_b16 v[238:239], v207 offset:16384
	ds_read_b64_tr_b16 v[240:241], v207 offset:18432
	s_waitcnt lgkmcnt(8)
	v_mfma_f32_16x16x32_bf16 v[130:133], v[162:165], v[210:213], v[130:133]
	v_mfma_f32_16x16x32_bf16 v[134:137], v[166:169], v[210:213], v[134:137]
	v_mfma_f32_16x16x32_bf16 v[138:141], v[218:221], v[210:213], v[138:141]
	v_mfma_f32_16x16x32_bf16 v[142:145], v[222:225], v[210:213], v[142:145]
	s_waitcnt lgkmcnt(5)
	v_mfma_f32_16x16x32_bf16 v[146:149], v[162:165], v[214:217], v[146:149]
	v_mfma_f32_16x16x32_bf16 v[150:153], v[166:169], v[214:217], v[150:153]
	ds_read_b128 v[162:165], v244 offset:2048
	ds_read_b64_tr_b16 v[166:167], v243 offset:16384
	ds_read_b64_tr_b16 v[168:169], v243 offset:18432
	v_mfma_f32_16x16x32_bf16 v[158:161], v[218:221], v[214:217], v[158:161]
	v_mfma_f32_16x16x32_bf16 v[154:157], v[222:225], v[214:217], v[154:157]
	ds_read_b128 v[208:211], v244 offset:4096
	s_waitcnt vmcnt(7)
	v_add_u32_e32 v206, s25, v206
	v_cvt_pk_bf16_f32 v30, v30, v31
	v_cvt_pk_bf16_f32 v31, v32, v33
	s_waitcnt lgkmcnt(6)
	v_mfma_f32_16x16x32_bf16 v[34:37], v[230:233], v[226:229], v[34:37]
	ds_write_b64 v206, v[30:31]
	v_mfma_f32_16x16x32_bf16 v[38:41], v[234:237], v[226:229], v[38:41]
	s_waitcnt lgkmcnt(5)
	v_mfma_f32_16x16x32_bf16 v[42:45], v[238:241], v[226:229], v[42:45]
	s_waitcnt lgkmcnt(2)
	v_mfma_f32_16x16x32_bf16 v[30:33], v[166:169], v[226:229], v[46:49]
	v_mfma_f32_16x16x32_bf16 v[46:49], v[230:233], v[162:165], v[50:53]
	v_add_u32_e32 v205, s25, v205
	v_mfma_f32_16x16x32_bf16 v[50:53], v[234:237], v[162:165], v[54:57]
	s_nop 2
	ds_read_b128 v[54:57], v244 offset:6144
	s_waitcnt vmcnt(6)
	v_mfma_f32_16x16x32_bf16 v[58:61], v[238:241], v[162:165], v[58:61]
	v_cvt_pk_bf16_f32 v26, v26, v27
	v_cvt_pk_bf16_f32 v27, v28, v29
	ds_write_b64 v205, v[26:27] offset:4096
	v_mfma_f32_16x16x32_bf16 v[26:29], v[166:169], v[162:165], v[62:65]
	s_waitcnt lgkmcnt(3)
	v_mfma_f32_16x16x32_bf16 v[62:65], v[230:233], v[208:211], v[66:69]
	v_mfma_f32_16x16x32_bf16 v[66:69], v[234:237], v[208:211], v[70:73]
	s_nop 2
	ds_read_b128 v[70:73], v244 offset:8192
	s_waitcnt vmcnt(5)
	v_mfma_f32_16x16x32_bf16 v[74:77], v[238:241], v[208:211], v[74:77]
	v_cvt_pk_bf16_f32 v22, v22, v23
	v_cvt_pk_bf16_f32 v23, v24, v25
	ds_write_b64 v206, v[22:23] offset:8192
	v_mfma_f32_16x16x32_bf16 v[22:25], v[166:169], v[208:211], v[78:81]
	s_waitcnt lgkmcnt(3)
	v_mfma_f32_16x16x32_bf16 v[78:81], v[230:233], v[54:57], v[82:85]
	v_mfma_f32_16x16x32_bf16 v[82:85], v[234:237], v[54:57], v[86:89]
	s_nop 2
	ds_read_b128 v[86:89], v244 offset:10240
	s_waitcnt vmcnt(4)
	v_mfma_f32_16x16x32_bf16 v[90:93], v[238:241], v[54:57], v[90:93]
	v_cvt_pk_bf16_f32 v18, v18, v19
	v_cvt_pk_bf16_f32 v19, v20, v21
	ds_write_b64 v205, v[18:19] offset:12288
	v_mfma_f32_16x16x32_bf16 v[18:21], v[166:169], v[54:57], v[94:97]
	s_waitcnt lgkmcnt(3)
	v_mfma_f32_16x16x32_bf16 v[54:57], v[230:233], v[70:73], v[98:101]
	s_nop 2
	ds_read_b128 v[98:101], v244 offset:12288
	s_waitcnt vmcnt(3)
	v_mfma_f32_16x16x32_bf16 v[94:97], v[234:237], v[70:73], v[102:105]
	v_cvt_pk_bf16_f32 v14, v14, v15
	v_cvt_pk_bf16_f32 v15, v16, v17
	ds_write_b64 v206, v[14:15] offset:16384
	v_mfma_f32_16x16x32_bf16 v[102:105], v[238:241], v[70:73], v[106:109]
	v_mfma_f32_16x16x32_bf16 v[14:17], v[166:169], v[70:73], v[110:113]
	s_nop 2
	ds_read_b128 v[110:113], v244 offset:14336
	s_waitcnt vmcnt(2)
	s_waitcnt lgkmcnt(4)
	v_mfma_f32_16x16x32_bf16 v[70:73], v[230:233], v[86:89], v[114:117]
	v_cvt_pk_bf16_f32 v10, v10, v11
	v_cvt_pk_bf16_f32 v11, v12, v13
	ds_write_b64 v205, v[10:11] offset:20480
	v_mfma_f32_16x16x32_bf16 v[106:109], v[234:237], v[86:89], v[118:121]
	v_mfma_f32_16x16x32_bf16 v[114:117], v[238:241], v[86:89], v[122:125]
	v_mfma_f32_16x16x32_bf16 v[10:13], v[166:169], v[86:89], v[126:129]
	s_waitcnt vmcnt(1)
	s_waitcnt lgkmcnt(3)
	v_mfma_f32_16x16x32_bf16 v[86:89], v[230:233], v[98:101], v[130:133]
	v_cvt_pk_bf16_f32 v6, v6, v7
	v_cvt_pk_bf16_f32 v7, v8, v9
	ds_write_b64 v206, v[6:7] offset:24576
	v_mfma_f32_16x16x32_bf16 v[118:121], v[234:237], v[98:101], v[134:137]
	v_mfma_f32_16x16x32_bf16 v[122:125], v[238:241], v[98:101], v[138:141]
	v_mfma_f32_16x16x32_bf16 v[6:9], v[166:169], v[98:101], v[142:145]
	s_waitcnt vmcnt(0)
	s_waitcnt lgkmcnt(2)
	v_mfma_f32_16x16x32_bf16 v[98:101], v[230:233], v[110:113], v[146:149]
	v_cvt_pk_bf16_f32 v2, v2, v3
	v_cvt_pk_bf16_f32 v3, v4, v5
	ds_write_b64 v205, v[2:3] offset:28672
	v_mfma_f32_16x16x32_bf16 v[126:129], v[234:237], v[110:113], v[150:153]
	v_mfma_f32_16x16x32_bf16 v[130:133], v[238:241], v[110:113], v[158:161]
	v_mfma_f32_16x16x32_bf16 v[2:5], v[166:169], v[110:113], v[154:157]
	s_waitcnt lgkmcnt(0)
	s_barrier
	v_add_u32_e32 v168, s25, v183
	v_add_u32_e32 v181, s25, v181
	v_add_u32_e32 v179, s25, v179
	ds_read_b64_tr_b16 v[110:111], v168
	ds_read_b64_tr_b16 v[112:113], v168 offset:2048
	ds_read_b64_tr_b16 v[134:135], v181
	ds_read_b64_tr_b16 v[136:137], v181 offset:2048
	ds_read_b128 v[138:141], v242 offset:32768
	ds_read_b64_tr_b16 v[142:143], v179
	ds_read_b128 v[146:149], v242 offset:34816
	ds_read_b128 v[150:153], v242 offset:36864
	ds_read_b64_tr_b16 v[144:145], v179 offset:2048
	v_add_u32_e32 v172, s25, v172
	ds_read_b64_tr_b16 v[154:155], v172
	ds_read_b64_tr_b16 v[156:157], v172 offset:2048
	s_waitcnt lgkmcnt(6)
	v_mfma_f32_16x16x32_bf16 v[34:37], v[110:113], v[138:141], v[34:37]
	v_mfma_f32_16x16x32_bf16 v[38:41], v[134:137], v[138:141], v[38:41]
	s_waitcnt lgkmcnt(2)
	v_mfma_f32_16x16x32_bf16 v[42:45], v[142:145], v[138:141], v[42:45]
	s_waitcnt lgkmcnt(0)
	v_mfma_f32_16x16x32_bf16 v[30:33], v[154:157], v[138:141], v[30:33]
	v_mfma_f32_16x16x32_bf16 v[46:49], v[110:113], v[146:149], v[46:49]
	ds_read_b128 v[138:141], v242 offset:38912
	v_mfma_f32_16x16x32_bf16 v[50:53], v[134:137], v[146:149], v[50:53]
	v_mfma_f32_16x16x32_bf16 v[58:61], v[142:145], v[146:149], v[58:61]
	v_mfma_f32_16x16x32_bf16 v[26:29], v[154:157], v[146:149], v[26:29]
	v_mfma_f32_16x16x32_bf16 v[62:65], v[110:113], v[150:153], v[62:65]
	ds_read_b128 v[146:149], v242 offset:40960
	v_mfma_f32_16x16x32_bf16 v[66:69], v[134:137], v[150:153], v[66:69]
	v_mfma_f32_16x16x32_bf16 v[74:77], v[142:145], v[150:153], v[74:77]
	v_mfma_f32_16x16x32_bf16 v[22:25], v[154:157], v[150:153], v[22:25]
	s_waitcnt lgkmcnt(1)
	v_mfma_f32_16x16x32_bf16 v[150:153], v[134:137], v[138:141], v[82:85]
	s_nop 2
	ds_read_b128 v[82:85], v242 offset:43008
	v_mfma_f32_16x16x32_bf16 v[78:81], v[110:113], v[138:141], v[78:81]
	v_mfma_f32_16x16x32_bf16 v[18:21], v[154:157], v[138:141], v[18:21]
	v_mfma_f32_16x16x32_bf16 v[158:161], v[142:145], v[138:141], v[90:93]
	s_nop 2
	ds_read_b128 v[90:93], v242 offset:45056
	ds_read_b64_tr_b16 v[166:167], v168 offset:16384
	ds_read_b64_tr_b16 v[168:169], v168 offset:18432
	s_waitcnt lgkmcnt(4)
	v_mfma_f32_16x16x32_bf16 v[54:57], v[110:113], v[146:149], v[54:57]
	v_mfma_f32_16x16x32_bf16 v[14:17], v[154:157], v[146:149], v[14:17]
	v_mfma_f32_16x16x32_bf16 v[138:141], v[134:137], v[146:149], v[94:97]
	v_mfma_f32_16x16x32_bf16 v[162:165], v[142:145], v[146:149], v[102:105]
	s_waitcnt lgkmcnt(3)
	v_mfma_f32_16x16x32_bf16 v[146:149], v[110:113], v[82:85], v[70:73]
	s_nop 2
	ds_read_b128 v[70:73], v242 offset:47104
	ds_read_b64_tr_b16 v[214:215], v181 offset:16384
	ds_read_b64_tr_b16 v[216:217], v181 offset:18432
	v_mfma_f32_16x16x32_bf16 v[10:13], v[154:157], v[82:85], v[10:13]
	v_mfma_f32_16x16x32_bf16 v[206:209], v[134:137], v[82:85], v[106:109]
	v_mfma_f32_16x16x32_bf16 v[210:213], v[142:145], v[82:85], v[114:117]
	ds_read_b128 v[82:85], v244 offset:32768
	ds_read_b64_tr_b16 v[230:231], v179 offset:16384
	ds_read_b64_tr_b16 v[232:233], v179 offset:18432
	s_waitcnt lgkmcnt(8)
	v_mfma_f32_16x16x32_bf16 v[6:9], v[154:157], v[90:93], v[6:9]
	v_mfma_f32_16x16x32_bf16 v[218:221], v[110:113], v[90:93], v[86:89]
	v_mfma_f32_16x16x32_bf16 v[222:225], v[134:137], v[90:93], v[118:121]
	v_mfma_f32_16x16x32_bf16 v[226:229], v[142:145], v[90:93], v[122:125]
	s_waitcnt lgkmcnt(5)
	v_mfma_f32_16x16x32_bf16 v[130:133], v[142:145], v[70:73], v[130:133]
	ds_read_b128 v[86:89], v244 offset:34816
	ds_read_b64_tr_b16 v[142:143], v172 offset:16384
	ds_read_b64_tr_b16 v[144:145], v172 offset:18432
	v_mfma_f32_16x16x32_bf16 v[134:137], v[134:137], v[70:73], v[126:129]
	v_mfma_f32_16x16x32_bf16 v[2:5], v[154:157], v[70:73], v[2:5]
	v_mfma_f32_16x16x32_bf16 v[234:237], v[110:113], v[70:73], v[98:101]
	s_waitcnt lgkmcnt(5)
	v_mfma_f32_16x16x32_bf16 v[126:129], v[166:169], v[82:85], v[34:37]
	s_nop 2
	ds_read_b128 v[34:37], v244 offset:36864
	v_mfma_f32_16x16x32_bf16 v[122:125], v[214:217], v[82:85], v[38:41]
	s_waitcnt lgkmcnt(4)
	v_mfma_f32_16x16x32_bf16 v[118:121], v[230:233], v[82:85], v[42:45]
	s_waitcnt lgkmcnt(1)
	v_mfma_f32_16x16x32_bf16 v[114:117], v[142:145], v[82:85], v[30:33]
	s_nop 2
	ds_read_b128 v[30:33], v244 offset:38912
	v_mfma_f32_16x16x32_bf16 v[110:113], v[166:169], v[86:89], v[46:49]
	v_mfma_f32_16x16x32_bf16 v[106:109], v[214:217], v[86:89], v[50:53]
	v_mfma_f32_16x16x32_bf16 v[102:105], v[230:233], v[86:89], v[58:61]
	v_mfma_f32_16x16x32_bf16 v[98:101], v[142:145], v[86:89], v[26:29]
	s_nop 2
	ds_read_b128 v[26:29], v244 offset:40960
	s_waitcnt lgkmcnt(2)
	v_mfma_f32_16x16x32_bf16 v[94:97], v[166:169], v[34:37], v[62:65]
	v_mfma_f32_16x16x32_bf16 v[90:93], v[214:217], v[34:37], v[66:69]
	v_mfma_f32_16x16x32_bf16 v[86:89], v[230:233], v[34:37], v[74:77]
	v_mfma_f32_16x16x32_bf16 v[82:85], v[142:145], v[34:37], v[22:25]
	s_nop 2
	ds_read_b128 v[22:25], v244 offset:43008
	s_waitcnt lgkmcnt(2)
	v_mfma_f32_16x16x32_bf16 v[78:81], v[166:169], v[30:33], v[78:81]
	v_mfma_f32_16x16x32_bf16 v[74:77], v[214:217], v[30:33], v[150:153]
	v_mfma_f32_16x16x32_bf16 v[70:73], v[230:233], v[30:33], v[158:161]
	v_mfma_f32_16x16x32_bf16 v[66:69], v[142:145], v[30:33], v[18:21]
	s_nop 2
	ds_read_b128 v[18:21], v244 offset:45056
	s_waitcnt lgkmcnt(2)
	v_mfma_f32_16x16x32_bf16 v[62:65], v[166:169], v[26:29], v[54:57]
	v_mfma_f32_16x16x32_bf16 v[58:61], v[214:217], v[26:29], v[138:141]
	v_mfma_f32_16x16x32_bf16 v[54:57], v[230:233], v[26:29], v[162:165]
	v_mfma_f32_16x16x32_bf16 v[50:53], v[142:145], v[26:29], v[14:17]
	s_waitcnt lgkmcnt(1)
	v_mfma_f32_16x16x32_bf16 v[46:49], v[166:169], v[22:25], v[146:149]
	ds_read_b128 v[138:141], v244 offset:47104
	v_mfma_f32_16x16x32_bf16 v[42:45], v[214:217], v[22:25], v[206:209]
	v_mfma_f32_16x16x32_bf16 v[38:41], v[230:233], v[22:25], v[210:213]
	v_mfma_f32_16x16x32_bf16 v[34:37], v[142:145], v[22:25], v[10:13]
	s_waitcnt lgkmcnt(1)
	v_mfma_f32_16x16x32_bf16 v[30:33], v[166:169], v[18:21], v[218:221]
	v_mfma_f32_16x16x32_bf16 v[26:29], v[214:217], v[18:21], v[222:225]
	v_mfma_f32_16x16x32_bf16 v[22:25], v[230:233], v[18:21], v[226:229]
	v_mfma_f32_16x16x32_bf16 v[18:21], v[142:145], v[18:21], v[6:9]
	s_waitcnt lgkmcnt(0)
	v_mfma_f32_16x16x32_bf16 v[14:17], v[166:169], v[138:141], v[234:237]
	v_mfma_f32_16x16x32_bf16 v[10:13], v[214:217], v[138:141], v[134:137]
	v_mfma_f32_16x16x32_bf16 v[6:9], v[230:233], v[138:141], v[130:133]
	v_mfma_f32_16x16x32_bf16 v[2:5], v[142:145], v[138:141], v[2:5]
	s_waitcnt lgkmcnt(0)
	s_barrier
	s_nop 0
	v_mov_b32_e32 v131, 0
	s_andn2_b64 vcc, exec, s[12:13]
	v_mov_b32_e32 v133, 0
	v_mov_b32_e32 v134, 0
	s_cbranch_vccnz .LBB0_1536
	global_load_dword v131, v[184:185], off
	global_load_dword v133, v[186:187], off
	global_load_dword v134, v[188:189], off
	s_branch .LBB0_1536
